# diff-attention output epilogue rewritten by hand: products in place, DPP+pack with one temporary, exec mask set once, 128 stores row by row (was ~11 instructions per 4-byte store)
# speedup vs baseline: 1.0045x; 1.0045x over previous
.Lmk_b1e:
	s_waitcnt vmcnt(8)
	s_waitcnt vmcnt(9)
	ds_write_b128 v0, v[194:197]
	s_waitcnt vmcnt(8)
	ds_write_b128 v0, v[198:201] offset:8192
	s_and_saveexec_b64 s[2:3], s[0:1]
	v_add_f32_e32 v0, v222, v223
	v_fmac_f32_e32 v0, v214, v221
	v_add_f32_e32 v158, v216, v217
	v_fmac_f32_e32 v158, v0, v215
	ds_write_b32 v212, v158
	s_or_b64 exec, exec, s[2:3]
	s_waitcnt lgkmcnt(0)
	ds_read_b128 v[190:193], v211
	s_ashr_i32 s65, s64, 31
	ds_read_b128 v[186:189], v211 offset:32
	ds_read_b128 v[182:185], v211 offset:64
	ds_read_b128 v[158:161], v211 offset:96
	s_lshl_b64 s[0:1], s[64:65], 13
	v_readlane_b32 s2, v254, 17
	s_waitcnt lgkmcnt(3)
	v_rcp_f32_e32 v190, v190
	v_readlane_b32 s3, v254, 18
	s_add_u32 s2, s2, s0
	v_and_b32_e32 v0, 1, v233
	s_addc_u32 s3, s3, s1
	v_cmp_eq_u32_e64 s[0:1], 0, v0
	v_lshlrev_b32_e32 v0, 1, v242
	v_lshl_add_u64 v[194:195], s[2:3], 0, v[0:1]
	v_lshlrev_b32_e32 v0, 15, v210
	v_lshl_add_u64 v[194:195], v[194:195], 0, v[0:1]
	s_waitcnt lgkmcnt(0)
	v_rcp_f32_e32 v191, v191
	v_rcp_f32_e32 v192, v192
	v_rcp_f32_e32 v193, v193
	v_rcp_f32_e32 v186, v186
	v_rcp_f32_e32 v187, v187
	v_rcp_f32_e32 v188, v188
	v_rcp_f32_e32 v189, v189
	v_rcp_f32_e32 v182, v182
	v_rcp_f32_e32 v183, v183
	v_rcp_f32_e32 v184, v184
	v_rcp_f32_e32 v185, v185
	v_rcp_f32_e32 v158, v158
	v_rcp_f32_e32 v159, v159
	v_rcp_f32_e32 v160, v160
	v_rcp_f32_e32 v161, v161
	s_nop 1
	v_mul_f32_e32 v114, v114, v190
	v_mul_f32_e32 v98, v98, v190
	v_mul_f32_e32 v82, v82, v190
	v_mul_f32_e32 v66, v66, v190
	v_mul_f32_e32 v50, v50, v190
	v_mul_f32_e32 v34, v34, v190
	v_mul_f32_e32 v18, v18, v190
	v_mul_f32_e32 v2, v2, v190
	v_mul_f32_e32 v115, v115, v191
	v_mul_f32_e32 v99, v99, v191
	v_mul_f32_e32 v83, v83, v191
	v_mul_f32_e32 v67, v67, v191
	v_mul_f32_e32 v51, v51, v191
	v_mul_f32_e32 v35, v35, v191
	v_mul_f32_e32 v19, v19, v191
	v_mul_f32_e32 v3, v3, v191
	v_mul_f32_e32 v116, v116, v192
	v_mul_f32_e32 v100, v100, v192
	v_mul_f32_e32 v84, v84, v192
	v_mul_f32_e32 v68, v68, v192
	v_mul_f32_e32 v52, v52, v192
	v_mul_f32_e32 v36, v36, v192
	v_mul_f32_e32 v20, v20, v192
	v_mul_f32_e32 v4, v4, v192
	v_mul_f32_e32 v117, v117, v193
	v_mul_f32_e32 v101, v101, v193
	v_mul_f32_e32 v85, v85, v193
	v_mul_f32_e32 v69, v69, v193
	v_mul_f32_e32 v53, v53, v193
	v_mul_f32_e32 v37, v37, v193
	v_mul_f32_e32 v21, v21, v193
	v_mul_f32_e32 v5, v5, v193
	v_mul_f32_e32 v118, v118, v186
	v_mul_f32_e32 v102, v102, v186
	v_mul_f32_e32 v86, v86, v186
	v_mul_f32_e32 v70, v70, v186
	v_mul_f32_e32 v54, v54, v186
	v_mul_f32_e32 v38, v38, v186
	v_mul_f32_e32 v22, v22, v186
	v_mul_f32_e32 v6, v6, v186
	v_mul_f32_e32 v119, v119, v187
	v_mul_f32_e32 v103, v103, v187
	v_mul_f32_e32 v87, v87, v187
	v_mul_f32_e32 v71, v71, v187
	v_mul_f32_e32 v55, v55, v187
	v_mul_f32_e32 v39, v39, v187
	v_mul_f32_e32 v23, v23, v187
	v_mul_f32_e32 v7, v7, v187
	v_mul_f32_e32 v120, v120, v188
	v_mul_f32_e32 v104, v104, v188
	v_mul_f32_e32 v88, v88, v188
	v_mul_f32_e32 v72, v72, v188
	v_mul_f32_e32 v56, v56, v188
	v_mul_f32_e32 v40, v40, v188
	v_mul_f32_e32 v24, v24, v188
	v_mul_f32_e32 v8, v8, v188
	v_mul_f32_e32 v121, v121, v189
	v_mul_f32_e32 v105, v105, v189
	v_mul_f32_e32 v89, v89, v189
	v_mul_f32_e32 v73, v73, v189
	v_mul_f32_e32 v57, v57, v189
	v_mul_f32_e32 v41, v41, v189
	v_mul_f32_e32 v25, v25, v189
	v_mul_f32_e32 v9, v9, v189
	v_mul_f32_e32 v122, v122, v182
	v_mul_f32_e32 v106, v106, v182
	v_mul_f32_e32 v90, v90, v182
	v_mul_f32_e32 v74, v74, v182
	v_mul_f32_e32 v58, v58, v182
	v_mul_f32_e32 v42, v42, v182
	v_mul_f32_e32 v26, v26, v182
	v_mul_f32_e32 v10, v10, v182
	v_mul_f32_e32 v123, v123, v183
	v_mul_f32_e32 v107, v107, v183
	v_mul_f32_e32 v91, v91, v183
	v_mul_f32_e32 v75, v75, v183
	v_mul_f32_e32 v59, v59, v183
	v_mul_f32_e32 v43, v43, v183
	v_mul_f32_e32 v27, v27, v183
	v_mul_f32_e32 v11, v11, v183
	v_mul_f32_e32 v124, v124, v184
	v_mul_f32_e32 v108, v108, v184
	v_mul_f32_e32 v92, v92, v184
	v_mul_f32_e32 v76, v76, v184
	v_mul_f32_e32 v60, v60, v184
	v_mul_f32_e32 v44, v44, v184
	v_mul_f32_e32 v28, v28, v184
	v_mul_f32_e32 v12, v12, v184
	v_mul_f32_e32 v125, v125, v185
	v_mul_f32_e32 v109, v109, v185
	v_mul_f32_e32 v93, v93, v185
	v_mul_f32_e32 v77, v77, v185
	v_mul_f32_e32 v61, v61, v185
	v_mul_f32_e32 v45, v45, v185
	v_mul_f32_e32 v29, v29, v185
	v_mul_f32_e32 v13, v13, v185
	v_mul_f32_e32 v126, v126, v158
	v_mul_f32_e32 v110, v110, v158
	v_mul_f32_e32 v94, v94, v158
	v_mul_f32_e32 v78, v78, v158
	v_mul_f32_e32 v62, v62, v158
	v_mul_f32_e32 v46, v46, v158
	v_mul_f32_e32 v30, v30, v158
	v_mul_f32_e32 v14, v14, v158
	v_mul_f32_e32 v127, v127, v159
	v_mul_f32_e32 v111, v111, v159
	v_mul_f32_e32 v95, v95, v159
	v_mul_f32_e32 v79, v79, v159
	v_mul_f32_e32 v63, v63, v159
	v_mul_f32_e32 v47, v47, v159
	v_mul_f32_e32 v31, v31, v159
	v_mul_f32_e32 v15, v15, v159
	v_mul_f32_e32 v128, v128, v160
	v_mul_f32_e32 v112, v112, v160
	v_mul_f32_e32 v96, v96, v160
	v_mul_f32_e32 v80, v80, v160
	v_mul_f32_e32 v64, v64, v160
	v_mul_f32_e32 v48, v48, v160
	v_mul_f32_e32 v32, v32, v160
	v_mul_f32_e32 v16, v16, v160
	v_mul_f32_e32 v129, v129, v161
	v_mul_f32_e32 v113, v113, v161
	v_mul_f32_e32 v97, v97, v161
	v_mul_f32_e32 v81, v81, v161
	v_mul_f32_e32 v65, v65, v161
	v_mul_f32_e32 v49, v49, v161
	v_mul_f32_e32 v33, v33, v161
	v_mul_f32_e32 v17, v17, v161
	v_mov_b32_dpp v0, v114 quad_perm:[1,0,3,2] row_mask:0xf bank_mask:0xf bound_ctrl:1
	v_cvt_pk_bf16_f32 v114, v114, v0
	v_mov_b32_dpp v0, v98 quad_perm:[1,0,3,2] row_mask:0xf bank_mask:0xf bound_ctrl:1
	v_cvt_pk_bf16_f32 v98, v98, v0
	v_mov_b32_dpp v0, v82 quad_perm:[1,0,3,2] row_mask:0xf bank_mask:0xf bound_ctrl:1
	v_cvt_pk_bf16_f32 v82, v82, v0
	v_mov_b32_dpp v0, v66 quad_perm:[1,0,3,2] row_mask:0xf bank_mask:0xf bound_ctrl:1
	v_cvt_pk_bf16_f32 v66, v66, v0
	v_mov_b32_dpp v0, v50 quad_perm:[1,0,3,2] row_mask:0xf bank_mask:0xf bound_ctrl:1
	v_cvt_pk_bf16_f32 v50, v50, v0
	v_mov_b32_dpp v0, v34 quad_perm:[1,0,3,2] row_mask:0xf bank_mask:0xf bound_ctrl:1
	v_cvt_pk_bf16_f32 v34, v34, v0
	v_mov_b32_dpp v0, v18 quad_perm:[1,0,3,2] row_mask:0xf bank_mask:0xf bound_ctrl:1
	v_cvt_pk_bf16_f32 v18, v18, v0
	v_mov_b32_dpp v0, v2 quad_perm:[1,0,3,2] row_mask:0xf bank_mask:0xf bound_ctrl:1
	v_cvt_pk_bf16_f32 v2, v2, v0
	v_mov_b32_dpp v0, v115 quad_perm:[1,0,3,2] row_mask:0xf bank_mask:0xf bound_ctrl:1
	v_cvt_pk_bf16_f32 v115, v115, v0
	v_mov_b32_dpp v0, v99 quad_perm:[1,0,3,2] row_mask:0xf bank_mask:0xf bound_ctrl:1
	v_cvt_pk_bf16_f32 v99, v99, v0
	v_mov_b32_dpp v0, v83 quad_perm:[1,0,3,2] row_mask:0xf bank_mask:0xf bound_ctrl:1
	v_cvt_pk_bf16_f32 v83, v83, v0
	v_mov_b32_dpp v0, v67 quad_perm:[1,0,3,2] row_mask:0xf bank_mask:0xf bound_ctrl:1
	v_cvt_pk_bf16_f32 v67, v67, v0
	v_mov_b32_dpp v0, v51 quad_perm:[1,0,3,2] row_mask:0xf bank_mask:0xf bound_ctrl:1
	v_cvt_pk_bf16_f32 v51, v51, v0
	v_mov_b32_dpp v0, v35 quad_perm:[1,0,3,2] row_mask:0xf bank_mask:0xf bound_ctrl:1
	v_cvt_pk_bf16_f32 v35, v35, v0
	v_mov_b32_dpp v0, v19 quad_perm:[1,0,3,2] row_mask:0xf bank_mask:0xf bound_ctrl:1
	v_cvt_pk_bf16_f32 v19, v19, v0
	v_mov_b32_dpp v0, v3 quad_perm:[1,0,3,2] row_mask:0xf bank_mask:0xf bound_ctrl:1
	v_cvt_pk_bf16_f32 v3, v3, v0
	v_mov_b32_dpp v0, v116 quad_perm:[1,0,3,2] row_mask:0xf bank_mask:0xf bound_ctrl:1
	v_cvt_pk_bf16_f32 v116, v116, v0
	v_mov_b32_dpp v0, v100 quad_perm:[1,0,3,2] row_mask:0xf bank_mask:0xf bound_ctrl:1
	v_cvt_pk_bf16_f32 v100, v100, v0
	v_mov_b32_dpp v0, v84 quad_perm:[1,0,3,2] row_mask:0xf bank_mask:0xf bound_ctrl:1
	v_cvt_pk_bf16_f32 v84, v84, v0
	v_mov_b32_dpp v0, v68 quad_perm:[1,0,3,2] row_mask:0xf bank_mask:0xf bound_ctrl:1
	v_cvt_pk_bf16_f32 v68, v68, v0
	v_mov_b32_dpp v0, v52 quad_perm:[1,0,3,2] row_mask:0xf bank_mask:0xf bound_ctrl:1
	v_cvt_pk_bf16_f32 v52, v52, v0
	v_mov_b32_dpp v0, v36 quad_perm:[1,0,3,2] row_mask:0xf bank_mask:0xf bound_ctrl:1
	v_cvt_pk_bf16_f32 v36, v36, v0
	v_mov_b32_dpp v0, v20 quad_perm:[1,0,3,2] row_mask:0xf bank_mask:0xf bound_ctrl:1
	v_cvt_pk_bf16_f32 v20, v20, v0
	v_mov_b32_dpp v0, v4 quad_perm:[1,0,3,2] row_mask:0xf bank_mask:0xf bound_ctrl:1
	v_cvt_pk_bf16_f32 v4, v4, v0
	v_mov_b32_dpp v0, v117 quad_perm:[1,0,3,2] row_mask:0xf bank_mask:0xf bound_ctrl:1
	v_cvt_pk_bf16_f32 v117, v117, v0
	v_mov_b32_dpp v0, v101 quad_perm:[1,0,3,2] row_mask:0xf bank_mask:0xf bound_ctrl:1
	v_cvt_pk_bf16_f32 v101, v101, v0
	v_mov_b32_dpp v0, v85 quad_perm:[1,0,3,2] row_mask:0xf bank_mask:0xf bound_ctrl:1
	v_cvt_pk_bf16_f32 v85, v85, v0
	v_mov_b32_dpp v0, v69 quad_perm:[1,0,3,2] row_mask:0xf bank_mask:0xf bound_ctrl:1
	v_cvt_pk_bf16_f32 v69, v69, v0
	v_mov_b32_dpp v0, v53 quad_perm:[1,0,3,2] row_mask:0xf bank_mask:0xf bound_ctrl:1
	v_cvt_pk_bf16_f32 v53, v53, v0
	v_mov_b32_dpp v0, v37 quad_perm:[1,0,3,2] row_mask:0xf bank_mask:0xf bound_ctrl:1
	v_cvt_pk_bf16_f32 v37, v37, v0
	v_mov_b32_dpp v0, v21 quad_perm:[1,0,3,2] row_mask:0xf bank_mask:0xf bound_ctrl:1
	v_cvt_pk_bf16_f32 v21, v21, v0
	v_mov_b32_dpp v0, v5 quad_perm:[1,0,3,2] row_mask:0xf bank_mask:0xf bound_ctrl:1
	v_cvt_pk_bf16_f32 v5, v5, v0
	v_mov_b32_dpp v0, v118 quad_perm:[1,0,3,2] row_mask:0xf bank_mask:0xf bound_ctrl:1
	v_cvt_pk_bf16_f32 v118, v118, v0
	v_mov_b32_dpp v0, v102 quad_perm:[1,0,3,2] row_mask:0xf bank_mask:0xf bound_ctrl:1
	v_cvt_pk_bf16_f32 v102, v102, v0
	v_mov_b32_dpp v0, v86 quad_perm:[1,0,3,2] row_mask:0xf bank_mask:0xf bound_ctrl:1
	v_cvt_pk_bf16_f32 v86, v86, v0
	v_mov_b32_dpp v0, v70 quad_perm:[1,0,3,2] row_mask:0xf bank_mask:0xf bound_ctrl:1
	v_cvt_pk_bf16_f32 v70, v70, v0
	v_mov_b32_dpp v0, v54 quad_perm:[1,0,3,2] row_mask:0xf bank_mask:0xf bound_ctrl:1
	v_cvt_pk_bf16_f32 v54, v54, v0
	v_mov_b32_dpp v0, v38 quad_perm:[1,0,3,2] row_mask:0xf bank_mask:0xf bound_ctrl:1
	v_cvt_pk_bf16_f32 v38, v38, v0
	v_mov_b32_dpp v0, v22 quad_perm:[1,0,3,2] row_mask:0xf bank_mask:0xf bound_ctrl:1
	v_cvt_pk_bf16_f32 v22, v22, v0
	v_mov_b32_dpp v0, v6 quad_perm:[1,0,3,2] row_mask:0xf bank_mask:0xf bound_ctrl:1
	v_cvt_pk_bf16_f32 v6, v6, v0
	v_mov_b32_dpp v0, v119 quad_perm:[1,0,3,2] row_mask:0xf bank_mask:0xf bound_ctrl:1
	v_cvt_pk_bf16_f32 v119, v119, v0
	v_mov_b32_dpp v0, v103 quad_perm:[1,0,3,2] row_mask:0xf bank_mask:0xf bound_ctrl:1
	v_cvt_pk_bf16_f32 v103, v103, v0
	v_mov_b32_dpp v0, v87 quad_perm:[1,0,3,2] row_mask:0xf bank_mask:0xf bound_ctrl:1
	v_cvt_pk_bf16_f32 v87, v87, v0
	v_mov_b32_dpp v0, v71 quad_perm:[1,0,3,2] row_mask:0xf bank_mask:0xf bound_ctrl:1
	v_cvt_pk_bf16_f32 v71, v71, v0
	v_mov_b32_dpp v0, v55 quad_perm:[1,0,3,2] row_mask:0xf bank_mask:0xf bound_ctrl:1
	v_cvt_pk_bf16_f32 v55, v55, v0
	v_mov_b32_dpp v0, v39 quad_perm:[1,0,3,2] row_mask:0xf bank_mask:0xf bound_ctrl:1
	v_cvt_pk_bf16_f32 v39, v39, v0
	v_mov_b32_dpp v0, v23 quad_perm:[1,0,3,2] row_mask:0xf bank_mask:0xf bound_ctrl:1
	v_cvt_pk_bf16_f32 v23, v23, v0
	v_mov_b32_dpp v0, v7 quad_perm:[1,0,3,2] row_mask:0xf bank_mask:0xf bound_ctrl:1
	v_cvt_pk_bf16_f32 v7, v7, v0
	v_mov_b32_dpp v0, v120 quad_perm:[1,0,3,2] row_mask:0xf bank_mask:0xf bound_ctrl:1
	v_cvt_pk_bf16_f32 v120, v120, v0
	v_mov_b32_dpp v0, v104 quad_perm:[1,0,3,2] row_mask:0xf bank_mask:0xf bound_ctrl:1
	v_cvt_pk_bf16_f32 v104, v104, v0
	v_mov_b32_dpp v0, v88 quad_perm:[1,0,3,2] row_mask:0xf bank_mask:0xf bound_ctrl:1
	v_cvt_pk_bf16_f32 v88, v88, v0
	v_mov_b32_dpp v0, v72 quad_perm:[1,0,3,2] row_mask:0xf bank_mask:0xf bound_ctrl:1
	v_cvt_pk_bf16_f32 v72, v72, v0
	v_mov_b32_dpp v0, v56 quad_perm:[1,0,3,2] row_mask:0xf bank_mask:0xf bound_ctrl:1
	v_cvt_pk_bf16_f32 v56, v56, v0
	v_mov_b32_dpp v0, v40 quad_perm:[1,0,3,2] row_mask:0xf bank_mask:0xf bound_ctrl:1
	v_cvt_pk_bf16_f32 v40, v40, v0
	v_mov_b32_dpp v0, v24 quad_perm:[1,0,3,2] row_mask:0xf bank_mask:0xf bound_ctrl:1
	v_cvt_pk_bf16_f32 v24, v24, v0
	v_mov_b32_dpp v0, v8 quad_perm:[1,0,3,2] row_mask:0xf bank_mask:0xf bound_ctrl:1
	v_cvt_pk_bf16_f32 v8, v8, v0
	v_mov_b32_dpp v0, v121 quad_perm:[1,0,3,2] row_mask:0xf bank_mask:0xf bound_ctrl:1
	v_cvt_pk_bf16_f32 v121, v121, v0
	v_mov_b32_dpp v0, v105 quad_perm:[1,0,3,2] row_mask:0xf bank_mask:0xf bound_ctrl:1
	v_cvt_pk_bf16_f32 v105, v105, v0
	v_mov_b32_dpp v0, v89 quad_perm:[1,0,3,2] row_mask:0xf bank_mask:0xf bound_ctrl:1
	v_cvt_pk_bf16_f32 v89, v89, v0
	v_mov_b32_dpp v0, v73 quad_perm:[1,0,3,2] row_mask:0xf bank_mask:0xf bound_ctrl:1
	v_cvt_pk_bf16_f32 v73, v73, v0
	v_mov_b32_dpp v0, v57 quad_perm:[1,0,3,2] row_mask:0xf bank_mask:0xf bound_ctrl:1
	v_cvt_pk_bf16_f32 v57, v57, v0
	v_mov_b32_dpp v0, v41 quad_perm:[1,0,3,2] row_mask:0xf bank_mask:0xf bound_ctrl:1
	v_cvt_pk_bf16_f32 v41, v41, v0
	v_mov_b32_dpp v0, v25 quad_perm:[1,0,3,2] row_mask:0xf bank_mask:0xf bound_ctrl:1
	v_cvt_pk_bf16_f32 v25, v25, v0
	v_mov_b32_dpp v0, v9 quad_perm:[1,0,3,2] row_mask:0xf bank_mask:0xf bound_ctrl:1
	v_cvt_pk_bf16_f32 v9, v9, v0
	v_mov_b32_dpp v0, v122 quad_perm:[1,0,3,2] row_mask:0xf bank_mask:0xf bound_ctrl:1
	v_cvt_pk_bf16_f32 v122, v122, v0
	v_mov_b32_dpp v0, v106 quad_perm:[1,0,3,2] row_mask:0xf bank_mask:0xf bound_ctrl:1
	v_cvt_pk_bf16_f32 v106, v106, v0
	v_mov_b32_dpp v0, v90 quad_perm:[1,0,3,2] row_mask:0xf bank_mask:0xf bound_ctrl:1
	v_cvt_pk_bf16_f32 v90, v90, v0
	v_mov_b32_dpp v0, v74 quad_perm:[1,0,3,2] row_mask:0xf bank_mask:0xf bound_ctrl:1
	v_cvt_pk_bf16_f32 v74, v74, v0
	v_mov_b32_dpp v0, v58 quad_perm:[1,0,3,2] row_mask:0xf bank_mask:0xf bound_ctrl:1
	v_cvt_pk_bf16_f32 v58, v58, v0
	v_mov_b32_dpp v0, v42 quad_perm:[1,0,3,2] row_mask:0xf bank_mask:0xf bound_ctrl:1
	v_cvt_pk_bf16_f32 v42, v42, v0
	v_mov_b32_dpp v0, v26 quad_perm:[1,0,3,2] row_mask:0xf bank_mask:0xf bound_ctrl:1
	v_cvt_pk_bf16_f32 v26, v26, v0
	v_mov_b32_dpp v0, v10 quad_perm:[1,0,3,2] row_mask:0xf bank_mask:0xf bound_ctrl:1
	v_cvt_pk_bf16_f32 v10, v10, v0
	v_mov_b32_dpp v0, v123 quad_perm:[1,0,3,2] row_mask:0xf bank_mask:0xf bound_ctrl:1
	v_cvt_pk_bf16_f32 v123, v123, v0
	v_mov_b32_dpp v0, v107 quad_perm:[1,0,3,2] row_mask:0xf bank_mask:0xf bound_ctrl:1
	v_cvt_pk_bf16_f32 v107, v107, v0
	v_mov_b32_dpp v0, v91 quad_perm:[1,0,3,2] row_mask:0xf bank_mask:0xf bound_ctrl:1
	v_cvt_pk_bf16_f32 v91, v91, v0
	v_mov_b32_dpp v0, v75 quad_perm:[1,0,3,2] row_mask:0xf bank_mask:0xf bound_ctrl:1
	v_cvt_pk_bf16_f32 v75, v75, v0
	v_mov_b32_dpp v0, v59 quad_perm:[1,0,3,2] row_mask:0xf bank_mask:0xf bound_ctrl:1
	v_cvt_pk_bf16_f32 v59, v59, v0
	v_mov_b32_dpp v0, v43 quad_perm:[1,0,3,2] row_mask:0xf bank_mask:0xf bound_ctrl:1
	v_cvt_pk_bf16_f32 v43, v43, v0
	v_mov_b32_dpp v0, v27 quad_perm:[1,0,3,2] row_mask:0xf bank_mask:0xf bound_ctrl:1
	v_cvt_pk_bf16_f32 v27, v27, v0
	v_mov_b32_dpp v0, v11 quad_perm:[1,0,3,2] row_mask:0xf bank_mask:0xf bound_ctrl:1
	v_cvt_pk_bf16_f32 v11, v11, v0
	v_mov_b32_dpp v0, v124 quad_perm:[1,0,3,2] row_mask:0xf bank_mask:0xf bound_ctrl:1
	v_cvt_pk_bf16_f32 v124, v124, v0
	v_mov_b32_dpp v0, v108 quad_perm:[1,0,3,2] row_mask:0xf bank_mask:0xf bound_ctrl:1
	v_cvt_pk_bf16_f32 v108, v108, v0
	v_mov_b32_dpp v0, v92 quad_perm:[1,0,3,2] row_mask:0xf bank_mask:0xf bound_ctrl:1
	v_cvt_pk_bf16_f32 v92, v92, v0
	v_mov_b32_dpp v0, v76 quad_perm:[1,0,3,2] row_mask:0xf bank_mask:0xf bound_ctrl:1
	v_cvt_pk_bf16_f32 v76, v76, v0
	v_mov_b32_dpp v0, v60 quad_perm:[1,0,3,2] row_mask:0xf bank_mask:0xf bound_ctrl:1
	v_cvt_pk_bf16_f32 v60, v60, v0
	v_mov_b32_dpp v0, v44 quad_perm:[1,0,3,2] row_mask:0xf bank_mask:0xf bound_ctrl:1
	v_cvt_pk_bf16_f32 v44, v44, v0
	v_mov_b32_dpp v0, v28 quad_perm:[1,0,3,2] row_mask:0xf bank_mask:0xf bound_ctrl:1
	v_cvt_pk_bf16_f32 v28, v28, v0
	v_mov_b32_dpp v0, v12 quad_perm:[1,0,3,2] row_mask:0xf bank_mask:0xf bound_ctrl:1
	v_cvt_pk_bf16_f32 v12, v12, v0
	v_mov_b32_dpp v0, v125 quad_perm:[1,0,3,2] row_mask:0xf bank_mask:0xf bound_ctrl:1
	v_cvt_pk_bf16_f32 v125, v125, v0
	v_mov_b32_dpp v0, v109 quad_perm:[1,0,3,2] row_mask:0xf bank_mask:0xf bound_ctrl:1
	v_cvt_pk_bf16_f32 v109, v109, v0
	v_mov_b32_dpp v0, v93 quad_perm:[1,0,3,2] row_mask:0xf bank_mask:0xf bound_ctrl:1
	v_cvt_pk_bf16_f32 v93, v93, v0
	v_mov_b32_dpp v0, v77 quad_perm:[1,0,3,2] row_mask:0xf bank_mask:0xf bound_ctrl:1
	v_cvt_pk_bf16_f32 v77, v77, v0
	v_mov_b32_dpp v0, v61 quad_perm:[1,0,3,2] row_mask:0xf bank_mask:0xf bound_ctrl:1
	v_cvt_pk_bf16_f32 v61, v61, v0
	v_mov_b32_dpp v0, v45 quad_perm:[1,0,3,2] row_mask:0xf bank_mask:0xf bound_ctrl:1
	v_cvt_pk_bf16_f32 v45, v45, v0
	v_mov_b32_dpp v0, v29 quad_perm:[1,0,3,2] row_mask:0xf bank_mask:0xf bound_ctrl:1
	v_cvt_pk_bf16_f32 v29, v29, v0
	v_mov_b32_dpp v0, v13 quad_perm:[1,0,3,2] row_mask:0xf bank_mask:0xf bound_ctrl:1
	v_cvt_pk_bf16_f32 v13, v13, v0
	v_mov_b32_dpp v0, v126 quad_perm:[1,0,3,2] row_mask:0xf bank_mask:0xf bound_ctrl:1
	v_cvt_pk_bf16_f32 v126, v126, v0
	v_mov_b32_dpp v0, v110 quad_perm:[1,0,3,2] row_mask:0xf bank_mask:0xf bound_ctrl:1
	v_cvt_pk_bf16_f32 v110, v110, v0
	v_mov_b32_dpp v0, v94 quad_perm:[1,0,3,2] row_mask:0xf bank_mask:0xf bound_ctrl:1
	v_cvt_pk_bf16_f32 v94, v94, v0
	v_mov_b32_dpp v0, v78 quad_perm:[1,0,3,2] row_mask:0xf bank_mask:0xf bound_ctrl:1
	v_cvt_pk_bf16_f32 v78, v78, v0
	v_mov_b32_dpp v0, v62 quad_perm:[1,0,3,2] row_mask:0xf bank_mask:0xf bound_ctrl:1
	v_cvt_pk_bf16_f32 v62, v62, v0
	v_mov_b32_dpp v0, v46 quad_perm:[1,0,3,2] row_mask:0xf bank_mask:0xf bound_ctrl:1
	v_cvt_pk_bf16_f32 v46, v46, v0
	v_mov_b32_dpp v0, v30 quad_perm:[1,0,3,2] row_mask:0xf bank_mask:0xf bound_ctrl:1
	v_cvt_pk_bf16_f32 v30, v30, v0
	v_mov_b32_dpp v0, v14 quad_perm:[1,0,3,2] row_mask:0xf bank_mask:0xf bound_ctrl:1
	v_cvt_pk_bf16_f32 v14, v14, v0
	v_mov_b32_dpp v0, v127 quad_perm:[1,0,3,2] row_mask:0xf bank_mask:0xf bound_ctrl:1
	v_cvt_pk_bf16_f32 v127, v127, v0
	v_mov_b32_dpp v0, v111 quad_perm:[1,0,3,2] row_mask:0xf bank_mask:0xf bound_ctrl:1
	v_cvt_pk_bf16_f32 v111, v111, v0
	v_mov_b32_dpp v0, v95 quad_perm:[1,0,3,2] row_mask:0xf bank_mask:0xf bound_ctrl:1
	v_cvt_pk_bf16_f32 v95, v95, v0
	v_mov_b32_dpp v0, v79 quad_perm:[1,0,3,2] row_mask:0xf bank_mask:0xf bound_ctrl:1
	v_cvt_pk_bf16_f32 v79, v79, v0
	v_mov_b32_dpp v0, v63 quad_perm:[1,0,3,2] row_mask:0xf bank_mask:0xf bound_ctrl:1
	v_cvt_pk_bf16_f32 v63, v63, v0
	v_mov_b32_dpp v0, v47 quad_perm:[1,0,3,2] row_mask:0xf bank_mask:0xf bound_ctrl:1
	v_cvt_pk_bf16_f32 v47, v47, v0
	v_mov_b32_dpp v0, v31 quad_perm:[1,0,3,2] row_mask:0xf bank_mask:0xf bound_ctrl:1
	v_cvt_pk_bf16_f32 v31, v31, v0
	v_mov_b32_dpp v0, v15 quad_perm:[1,0,3,2] row_mask:0xf bank_mask:0xf bound_ctrl:1
	v_cvt_pk_bf16_f32 v15, v15, v0
	v_mov_b32_dpp v0, v128 quad_perm:[1,0,3,2] row_mask:0xf bank_mask:0xf bound_ctrl:1
	v_cvt_pk_bf16_f32 v128, v128, v0
	v_mov_b32_dpp v0, v112 quad_perm:[1,0,3,2] row_mask:0xf bank_mask:0xf bound_ctrl:1
	v_cvt_pk_bf16_f32 v112, v112, v0
	v_mov_b32_dpp v0, v96 quad_perm:[1,0,3,2] row_mask:0xf bank_mask:0xf bound_ctrl:1
	v_cvt_pk_bf16_f32 v96, v96, v0
	v_mov_b32_dpp v0, v80 quad_perm:[1,0,3,2] row_mask:0xf bank_mask:0xf bound_ctrl:1
	v_cvt_pk_bf16_f32 v80, v80, v0
	v_mov_b32_dpp v0, v64 quad_perm:[1,0,3,2] row_mask:0xf bank_mask:0xf bound_ctrl:1
	v_cvt_pk_bf16_f32 v64, v64, v0
	v_mov_b32_dpp v0, v48 quad_perm:[1,0,3,2] row_mask:0xf bank_mask:0xf bound_ctrl:1
	v_cvt_pk_bf16_f32 v48, v48, v0
	v_mov_b32_dpp v0, v32 quad_perm:[1,0,3,2] row_mask:0xf bank_mask:0xf bound_ctrl:1
	v_cvt_pk_bf16_f32 v32, v32, v0
	v_mov_b32_dpp v0, v16 quad_perm:[1,0,3,2] row_mask:0xf bank_mask:0xf bound_ctrl:1
	v_cvt_pk_bf16_f32 v16, v16, v0
	v_mov_b32_dpp v0, v129 quad_perm:[1,0,3,2] row_mask:0xf bank_mask:0xf bound_ctrl:1
	v_cvt_pk_bf16_f32 v129, v129, v0
	v_mov_b32_dpp v0, v113 quad_perm:[1,0,3,2] row_mask:0xf bank_mask:0xf bound_ctrl:1
	v_cvt_pk_bf16_f32 v113, v113, v0
	v_mov_b32_dpp v0, v97 quad_perm:[1,0,3,2] row_mask:0xf bank_mask:0xf bound_ctrl:1
	v_cvt_pk_bf16_f32 v97, v97, v0
	v_mov_b32_dpp v0, v81 quad_perm:[1,0,3,2] row_mask:0xf bank_mask:0xf bound_ctrl:1
	v_cvt_pk_bf16_f32 v81, v81, v0
	v_mov_b32_dpp v0, v65 quad_perm:[1,0,3,2] row_mask:0xf bank_mask:0xf bound_ctrl:1
	v_cvt_pk_bf16_f32 v65, v65, v0
	v_mov_b32_dpp v0, v49 quad_perm:[1,0,3,2] row_mask:0xf bank_mask:0xf bound_ctrl:1
	v_cvt_pk_bf16_f32 v49, v49, v0
	v_mov_b32_dpp v0, v33 quad_perm:[1,0,3,2] row_mask:0xf bank_mask:0xf bound_ctrl:1
	v_cvt_pk_bf16_f32 v33, v33, v0
	v_mov_b32_dpp v0, v17 quad_perm:[1,0,3,2] row_mask:0xf bank_mask:0xf bound_ctrl:1
	v_cvt_pk_bf16_f32 v17, v17, v0
	s_mov_b64 exec, s[0:1]
	global_store_dword v[194:195], v114, off
	global_store_dword v[194:195], v98, off offset:64
	global_store_dword v[194:195], v82, off offset:128
	global_store_dword v[194:195], v66, off offset:192
	global_store_dword v[194:195], v50, off offset:256
	global_store_dword v[194:195], v34, off offset:320
	global_store_dword v[194:195], v18, off offset:384
	global_store_dword v[194:195], v2, off offset:448
	s_mov_b64 s[2:3], 0x2000
	v_lshl_add_u64 v[190:191], v[194:195], 0, s[2:3]
	global_store_dword v[190:191], v115, off
	global_store_dword v[190:191], v99, off offset:64
	global_store_dword v[190:191], v83, off offset:128
	global_store_dword v[190:191], v67, off offset:192
	global_store_dword v[190:191], v51, off offset:256
	global_store_dword v[190:191], v35, off offset:320
	global_store_dword v[190:191], v19, off offset:384
	global_store_dword v[190:191], v3, off offset:448
	s_mov_b64 s[2:3], 0x4000
	v_lshl_add_u64 v[192:193], v[194:195], 0, s[2:3]
	global_store_dword v[192:193], v116, off
	global_store_dword v[192:193], v100, off offset:64
	global_store_dword v[192:193], v84, off offset:128
	global_store_dword v[192:193], v68, off offset:192
	global_store_dword v[192:193], v52, off offset:256
	global_store_dword v[192:193], v36, off offset:320
	global_store_dword v[192:193], v20, off offset:384
	global_store_dword v[192:193], v4, off offset:448
	s_mov_b64 s[2:3], 0x6000
	v_lshl_add_u64 v[190:191], v[194:195], 0, s[2:3]
	global_store_dword v[190:191], v117, off
	global_store_dword v[190:191], v101, off offset:64
	global_store_dword v[190:191], v85, off offset:128
	global_store_dword v[190:191], v69, off offset:192
	global_store_dword v[190:191], v53, off offset:256
	global_store_dword v[190:191], v37, off offset:320
	global_store_dword v[190:191], v21, off offset:384
	global_store_dword v[190:191], v5, off offset:448
	s_mov_b64 s[2:3], 0x10000
	v_lshl_add_u64 v[192:193], v[194:195], 0, s[2:3]
	global_store_dword v[192:193], v118, off
	global_store_dword v[192:193], v102, off offset:64
	global_store_dword v[192:193], v86, off offset:128
	global_store_dword v[192:193], v70, off offset:192
	global_store_dword v[192:193], v54, off offset:256
	global_store_dword v[192:193], v38, off offset:320
	global_store_dword v[192:193], v22, off offset:384
	global_store_dword v[192:193], v6, off offset:448
	s_mov_b64 s[2:3], 0x12000
	v_lshl_add_u64 v[190:191], v[194:195], 0, s[2:3]
	global_store_dword v[190:191], v119, off
	global_store_dword v[190:191], v103, off offset:64
	global_store_dword v[190:191], v87, off offset:128
	global_store_dword v[190:191], v71, off offset:192
	global_store_dword v[190:191], v55, off offset:256
	global_store_dword v[190:191], v39, off offset:320
	global_store_dword v[190:191], v23, off offset:384
	global_store_dword v[190:191], v7, off offset:448
	s_mov_b64 s[2:3], 0x14000
	v_lshl_add_u64 v[192:193], v[194:195], 0, s[2:3]
	global_store_dword v[192:193], v120, off
	global_store_dword v[192:193], v104, off offset:64
	global_store_dword v[192:193], v88, off offset:128
	global_store_dword v[192:193], v72, off offset:192
	global_store_dword v[192:193], v56, off offset:256
	global_store_dword v[192:193], v40, off offset:320
	global_store_dword v[192:193], v24, off offset:384
	global_store_dword v[192:193], v8, off offset:448
	s_mov_b64 s[2:3], 0x16000
	v_lshl_add_u64 v[190:191], v[194:195], 0, s[2:3]
	global_store_dword v[190:191], v121, off
	global_store_dword v[190:191], v105, off offset:64
	global_store_dword v[190:191], v89, off offset:128
	global_store_dword v[190:191], v73, off offset:192
	global_store_dword v[190:191], v57, off offset:256
	global_store_dword v[190:191], v41, off offset:320
	global_store_dword v[190:191], v25, off offset:384
	global_store_dword v[190:191], v9, off offset:448
	s_mov_b64 s[2:3], 0x20000
	v_lshl_add_u64 v[192:193], v[194:195], 0, s[2:3]
	global_store_dword v[192:193], v122, off
	global_store_dword v[192:193], v106, off offset:64
	global_store_dword v[192:193], v90, off offset:128
	global_store_dword v[192:193], v74, off offset:192
	global_store_dword v[192:193], v58, off offset:256
	global_store_dword v[192:193], v42, off offset:320
	global_store_dword v[192:193], v26, off offset:384
	global_store_dword v[192:193], v10, off offset:448
	s_mov_b64 s[2:3], 0x22000
	v_lshl_add_u64 v[190:191], v[194:195], 0, s[2:3]
	global_store_dword v[190:191], v123, off
	global_store_dword v[190:191], v107, off offset:64
	global_store_dword v[190:191], v91, off offset:128
	global_store_dword v[190:191], v75, off offset:192
	global_store_dword v[190:191], v59, off offset:256
	global_store_dword v[190:191], v43, off offset:320
	global_store_dword v[190:191], v27, off offset:384
	global_store_dword v[190:191], v11, off offset:448
	s_mov_b64 s[2:3], 0x24000
	v_lshl_add_u64 v[192:193], v[194:195], 0, s[2:3]
	global_store_dword v[192:193], v124, off
	global_store_dword v[192:193], v108, off offset:64
	global_store_dword v[192:193], v92, off offset:128
	global_store_dword v[192:193], v76, off offset:192
	global_store_dword v[192:193], v60, off offset:256
	global_store_dword v[192:193], v44, off offset:320
	global_store_dword v[192:193], v28, off offset:384
	global_store_dword v[192:193], v12, off offset:448
	s_mov_b64 s[2:3], 0x26000
	v_lshl_add_u64 v[190:191], v[194:195], 0, s[2:3]
	global_store_dword v[190:191], v125, off
	global_store_dword v[190:191], v109, off offset:64
	global_store_dword v[190:191], v93, off offset:128
	global_store_dword v[190:191], v77, off offset:192
	global_store_dword v[190:191], v61, off offset:256
	global_store_dword v[190:191], v45, off offset:320
	global_store_dword v[190:191], v29, off offset:384
	global_store_dword v[190:191], v13, off offset:448
	s_mov_b64 s[2:3], 0x30000
	v_lshl_add_u64 v[192:193], v[194:195], 0, s[2:3]
	global_store_dword v[192:193], v126, off
	global_store_dword v[192:193], v110, off offset:64
	global_store_dword v[192:193], v94, off offset:128
	global_store_dword v[192:193], v78, off offset:192
	global_store_dword v[192:193], v62, off offset:256
	global_store_dword v[192:193], v46, off offset:320
	global_store_dword v[192:193], v30, off offset:384
	global_store_dword v[192:193], v14, off offset:448
	s_mov_b64 s[2:3], 0x32000
	v_lshl_add_u64 v[190:191], v[194:195], 0, s[2:3]
	global_store_dword v[190:191], v127, off
	global_store_dword v[190:191], v111, off offset:64
	global_store_dword v[190:191], v95, off offset:128
	global_store_dword v[190:191], v79, off offset:192
	global_store_dword v[190:191], v63, off offset:256
	global_store_dword v[190:191], v47, off offset:320
	global_store_dword v[190:191], v31, off offset:384
	global_store_dword v[190:191], v15, off offset:448
	s_mov_b64 s[2:3], 0x34000
	v_lshl_add_u64 v[192:193], v[194:195], 0, s[2:3]
	global_store_dword v[192:193], v128, off
	global_store_dword v[192:193], v112, off offset:64
	global_store_dword v[192:193], v96, off offset:128
	global_store_dword v[192:193], v80, off offset:192
	global_store_dword v[192:193], v64, off offset:256
	global_store_dword v[192:193], v48, off offset:320
	global_store_dword v[192:193], v32, off offset:384
	global_store_dword v[192:193], v16, off offset:448
	s_mov_b64 s[2:3], 0x36000
	v_lshl_add_u64 v[190:191], v[194:195], 0, s[2:3]
	global_store_dword v[190:191], v129, off
	global_store_dword v[190:191], v113, off offset:64
	global_store_dword v[190:191], v97, off offset:128
	global_store_dword v[190:191], v81, off offset:192
	global_store_dword v[190:191], v65, off offset:256
	global_store_dword v[190:191], v49, off offset:320
	global_store_dword v[190:191], v33, off offset:384
	global_store_dword v[190:191], v17, off offset:448
	s_mov_b64 exec, -1
	s_mov_b64 s[2:3], 0
	s_branch .LBB0_1348
